# adds: NSA tile loop keeps the first-half scores in the MFMA output registers (no copies, masks in place, no-rescale exponentials straight from them)
# baseline (speedup 1.0000x reference)
.LBB0_2419:
	s_lshl_b32 s2, s2, 13
	s_add_i32 s76, s2, 0
	s_add_i32 s76, s76, 0x10000
	s_andn2_b64 vcc, exec, s[8:9]
	v_lshlrev_b32_e32 v134, 2, v162
	s_cbranch_vccnz .LBB0_2468
	v_or_b32_e32 v6, 32, v168
	v_cmp_gt_i32_e64 s[40:41], v6, v2
	v_cmp_lt_i32_e64 s[42:43], v6, v2
	v_or_b32_e32 v6, 34, v168
	v_cmp_gt_i32_e64 s[44:45], v6, v2
	v_or_b32_e32 v6, 35, v168
	v_cmp_gt_i32_e64 s[46:47], v6, v2
	v_or_b32_e32 v6, 40, v168
	v_cmp_gt_i32_e64 s[48:49], v6, v2
	v_or_b32_e32 v6, 41, v168
	v_cmp_gt_i32_e64 s[50:51], v6, v2
	v_or_b32_e32 v6, 42, v168
	v_cmp_gt_i32_e64 s[52:53], v6, v2
	v_or_b32_e32 v6, 43, v168
	v_cmp_gt_i32_e64 s[54:55], v6, v2
	v_or_b32_e32 v6, 48, v168
	v_cmp_gt_i32_e64 s[56:57], v6, v2
	v_or_b32_e32 v6, 49, v168
	v_cmp_gt_i32_e64 s[58:59], v6, v2
	v_or_b32_e32 v6, 50, v168
	v_cmp_gt_i32_e64 s[60:61], v6, v2
	v_or_b32_e32 v6, 51, v168
	v_cmp_gt_i32_e64 s[62:63], v6, v2
	v_or_b32_e32 v6, 56, v168
	v_cmp_gt_i32_e64 s[64:65], v6, v2
	v_or_b32_e32 v6, 57, v168
	v_cmp_gt_i32_e64 s[66:67], v6, v2
	v_or_b32_e32 v6, 58, v168
	v_cmp_gt_i32_e64 s[68:69], v6, v2
	v_or_b32_e32 v6, 59, v168
	v_cmp_gt_i32_e64 s[6:7], v168, v2
	v_cmp_lt_i32_e64 s[8:9], v168, v2
	v_cmp_gt_i32_e64 s[10:11], v135, v2
	v_cmp_gt_i32_e64 s[12:13], v169, v2
	v_cmp_gt_i32_e64 s[14:15], v170, v2
	v_cmp_gt_i32_e64 s[16:17], v171, v2
	v_cmp_gt_i32_e64 s[18:19], v172, v2
	v_cmp_gt_i32_e64 s[20:21], v173, v2
	v_cmp_gt_i32_e64 s[22:23], v174, v2
	v_cmp_gt_i32_e64 s[24:25], v175, v2
	v_cmp_gt_i32_e64 s[26:27], v176, v2
	v_cmp_gt_i32_e64 s[28:29], v177, v2
	v_cmp_gt_i32_e64 s[30:31], v178, v2
	v_cmp_gt_i32_e64 s[34:35], v179, v2
	v_cmp_gt_i32_e64 s[36:37], v180, v2
	v_cmp_gt_i32_e64 s[38:39], v181, v2
	v_cmp_gt_i32_e64 s[70:71], v6, v2
	s_min_u32 s2, s92, 8
	v_lshlrev_b32_e32 v2, 4, v4
	s_add_i32 s2, s92, s2
	v_and_b32_e32 v2, 0xc0, v2
	s_lshl_b32 s87, s2, 13
	v_lshl_or_b32 v2, v160, 8, v2
	v_readlane_b32 s2, v247, 4
	v_lshlrev_b32_e32 v5, 1, v4
	v_mov_b32_e32 v140, 0
	v_add_u32_e32 v185, s2, v2
	v_readlane_b32 s2, v247, 5
	s_movk_i32 s96, 0xc00
	s_add_i32 s91, s91, s92
	v_add_u32_e32 v187, s2, v2
	v_readlane_b32 s2, v247, 6
	s_add_i32 s93, s93, s3
	v_mov_b32_e32 v139, v131
	v_add_u32_e32 v188, s2, v2
	v_readlane_b32 s2, v247, 7
	s_mov_b32 s94, 2
	v_add_u32_e32 v183, s75, v134
	v_add_u32_e32 v189, s2, v2
	v_readlane_b32 s2, v247, 8
	v_add3_u32 v184, s76, v166, v134
	s_lshl_b32 s95, s92, 13
	v_add_u32_e32 v190, s2, v2
	v_readlane_b32 s2, v247, 9
	s_addk_i32 s87, 0x4000
	v_and_or_b32 v186, v5, 32, v3
	v_add_u32_e32 v191, s2, v2
	v_readlane_b32 s2, v247, 10
	s_add_i32 s86, s75, 0xc000
	s_mov_b32 s3, 0
	v_add_u32_e32 v192, s2, v2
	v_readlane_b32 s2, v247, 11
	v_mov_b32_e32 v202, 0
	v_mov_b32_e32 v3, v140
	v_add_u32_e32 v193, s2, v2
	v_readlane_b32 s2, v247, 12
	v_mov_b32_e32 v4, v140
	v_mov_b32_e32 v5, v140
	v_add_u32_e32 v194, s2, v2
	v_readlane_b32 s2, v247, 13
	v_mov_b32_e32 v6, v140
	v_mov_b32_e32 v7, v140
	v_add_u32_e32 v195, s2, v2
	v_readlane_b32 s2, v247, 14
	v_mov_b32_e32 v8, v140
	v_mov_b32_e32 v9, v140
	v_add_u32_e32 v196, s2, v2
	v_readlane_b32 s2, v247, 15
	v_mov_b32_e32 v10, v140
	v_mov_b32_e32 v11, v140
	v_add_u32_e32 v197, s2, v2
	v_readlane_b32 s2, v247, 16
	v_mov_b32_e32 v12, v140
	v_mov_b32_e32 v13, v140
	v_add_u32_e32 v198, s2, v2
	v_readlane_b32 s2, v247, 17
	v_mov_b32_e32 v14, v140
	v_mov_b32_e32 v15, v140
	v_add_u32_e32 v199, s2, v2
	v_readlane_b32 s2, v247, 21
	v_mov_b32_e32 v16, v140
	v_mov_b32_e32 v17, v140
	v_add_u32_e32 v200, s2, v2
	s_add_i32 s2, 0, 0x8000
	v_add_u32_e32 v201, s2, v2
	s_mov_b32 s2, 0
	v_mov_b32_e32 v2, 0
	v_mov_b32_e32 v18, 0
	v_mov_b32_e32 v19, v140
	v_mov_b32_e32 v20, v140
	v_mov_b32_e32 v21, v140
	v_mov_b32_e32 v22, v140
	v_mov_b32_e32 v23, v140
	v_add_u32_e32 v226, v201, v186
	v_mov_b32_e32 v24, v140
	v_mov_b32_e32 v25, v140
	v_mov_b32_e32 v26, v140
	v_mov_b32_e32 v27, v140
	v_mov_b32_e32 v28, v140
	v_mov_b32_e32 v29, v140
	v_mov_b32_e32 v30, v140
	v_mov_b32_e32 v31, v140
	v_mov_b32_e32 v32, v140
	v_mov_b32_e32 v33, v140
	v_mov_b64_e32 v[50:51], v[98:99]
	v_mov_b64_e32 v[52:53], v[100:101]
	v_mov_b64_e32 v[54:55], v[102:103]
	v_mov_b64_e32 v[56:57], v[104:105]
	v_mov_b64_e32 v[58:59], v[106:107]
	v_mov_b64_e32 v[60:61], v[108:109]
	v_mov_b64_e32 v[62:63], v[110:111]
	v_mov_b64_e32 v[64:65], v[112:113]
	s_branch .LBB0_2422
.LBB0_2421:
	s_or_b64 exec, exec, s[72:73]
	s_waitcnt lgkmcnt(0)
	v_add_u32_e32 v34, s75, v136
	ds_read_b32 v35, v34 offset:57472
	v_pk_add_f32 v[64:65], v[140:141], v[64:65] op_sel_hi:[0,1]
	v_pk_add_f32 v[62:63], v[140:141], v[62:63] op_sel_hi:[0,1]
	v_pk_add_f32 v[60:61], v[140:141], v[60:61] op_sel_hi:[0,1]
	v_pk_add_f32 v[58:59], v[140:141], v[58:59] op_sel_hi:[0,1]
	s_waitcnt lgkmcnt(0)
	v_mul_f32_e32 v2, v2, v35
	v_mul_f32_e32 v18, v18, v35
	ds_write2_b32 v184, v2, v18 offset1:32
	ds_read_b32 v2, v34 offset:57476
	v_pk_add_f32 v[56:57], v[140:141], v[56:57] op_sel_hi:[0,1]
	v_pk_add_f32 v[54:55], v[140:141], v[54:55] op_sel_hi:[0,1]
	v_pk_add_f32 v[52:53], v[140:141], v[52:53] op_sel_hi:[0,1]
	v_pk_add_f32 v[50:51], v[140:141], v[50:51] op_sel_hi:[0,1]
	s_waitcnt lgkmcnt(0)
	v_mul_f32_e32 v3, v3, v2
	v_mul_f32_e32 v2, v19, v2
	ds_write2_b32 v184, v3, v2 offset0:64 offset1:96
	ds_read_b32 v2, v34 offset:57480
	s_waitcnt lgkmcnt(0)
	v_mul_f32_e32 v3, v4, v2
	v_mul_f32_e32 v2, v20, v2
	ds_write2_b32 v184, v3, v2 offset0:128 offset1:160
	ds_read_b32 v2, v34 offset:57484
	v_add_u32_e32 v4, 0x800, v184
	s_waitcnt lgkmcnt(0)
	v_mul_f32_e32 v3, v5, v2
	v_mul_f32_e32 v2, v21, v2
	ds_write2_b32 v184, v3, v2 offset0:192 offset1:224
	ds_read_b32 v2, v34 offset:57504
	s_waitcnt lgkmcnt(0)
	v_mul_f32_e32 v3, v6, v2
	v_mul_f32_e32 v2, v22, v2
	ds_write2_b32 v4, v3, v2 offset1:32
	ds_read_b32 v2, v34 offset:57508
	s_waitcnt lgkmcnt(0)
	v_mul_f32_e32 v3, v7, v2
	v_mul_f32_e32 v2, v23, v2
	ds_write2_b32 v4, v3, v2 offset0:64 offset1:96
	ds_read_b32 v2, v34 offset:57512
	s_waitcnt lgkmcnt(0)
	v_mul_f32_e32 v3, v8, v2
	v_mul_f32_e32 v2, v24, v2
	ds_write2_b32 v4, v3, v2 offset0:128 offset1:160
	ds_read_b32 v2, v34 offset:57516
	s_waitcnt lgkmcnt(0)
	v_mul_f32_e32 v3, v9, v2
	v_mul_f32_e32 v2, v25, v2
	ds_write2_b32 v4, v3, v2 offset0:192 offset1:224
	ds_read_b32 v2, v34 offset:57536
	v_add_u32_e32 v4, 0x1000, v184
	s_waitcnt lgkmcnt(0)
	v_mul_f32_e32 v3, v10, v2
	v_mul_f32_e32 v2, v26, v2
	ds_write2_b32 v4, v3, v2 offset1:32
	ds_read_b32 v2, v34 offset:57540
	s_waitcnt lgkmcnt(0)
	v_mul_f32_e32 v3, v11, v2
	v_mul_f32_e32 v2, v27, v2
	ds_write2_b32 v4, v3, v2 offset0:64 offset1:96
	ds_read_b32 v2, v34 offset:57544
	s_waitcnt lgkmcnt(0)
	v_mul_f32_e32 v3, v12, v2
	v_mul_f32_e32 v2, v28, v2
	ds_write2_b32 v4, v3, v2 offset0:128 offset1:160
	ds_read_b32 v2, v34 offset:57548
	s_waitcnt lgkmcnt(0)
	v_mul_f32_e32 v3, v13, v2
	v_mul_f32_e32 v2, v29, v2
	ds_write2_b32 v4, v3, v2 offset0:192 offset1:224
	ds_read_b32 v2, v34 offset:57568
	v_add_u32_e32 v4, 0x1800, v184
	s_waitcnt lgkmcnt(0)
	v_mul_f32_e32 v3, v14, v2
	v_mul_f32_e32 v2, v30, v2
	ds_write2_b32 v4, v3, v2 offset1:32
	ds_read_b32 v2, v34 offset:57572
	s_waitcnt lgkmcnt(0)
	v_mul_f32_e32 v3, v15, v2
	v_mul_f32_e32 v2, v31, v2
	ds_write2_b32 v4, v3, v2 offset0:64 offset1:96
	ds_read_b32 v2, v34 offset:57576
	s_waitcnt lgkmcnt(0)
	v_mul_f32_e32 v3, v16, v2
	v_mul_f32_e32 v2, v32, v2
	ds_write2_b32 v4, v3, v2 offset0:128 offset1:160
	ds_read_b32 v2, v34 offset:57580
	v_mov_b64_e32 v[34:35], v[66:67]
	v_mov_b64_e32 v[36:37], v[68:69]
	v_mov_b64_e32 v[38:39], v[70:71]
	v_mov_b64_e32 v[40:41], v[72:73]
	s_waitcnt lgkmcnt(0)
	v_mul_f32_e32 v3, v17, v2
	v_mul_f32_e32 v2, v33, v2
	ds_write2_b32 v4, v3, v2 offset0:192 offset1:224
	s_waitcnt lgkmcnt(0)
	v_mov_b32_e32 v17, 0
	v_mov_b64_e32 v[42:43], v[74:75]
	v_mov_b64_e32 v[44:45], v[76:77]
	v_mov_b64_e32 v[46:47], v[78:79]
	v_mov_b64_e32 v[48:49], v[80:81]
	v_mov_b32_e32 v16, v17
	v_mov_b32_e32 v15, v17
	v_mov_b32_e32 v14, v17
	v_mov_b32_e32 v13, v17
	v_mov_b32_e32 v12, v17
	v_mov_b32_e32 v11, v17
	v_mov_b32_e32 v10, v17
	v_mov_b32_e32 v9, v17
	v_mov_b32_e32 v8, v17
	v_mov_b32_e32 v7, v17
	v_mov_b32_e32 v6, v17
	v_mov_b32_e32 v5, v17
	v_mov_b32_e32 v4, v17
	v_mov_b32_e32 v3, v17
	v_mov_b32_e32 v2, v17
	v_mov_b32_e32 v33, v17
	v_mov_b32_e32 v32, v17
	v_mov_b32_e32 v31, v17
	v_mov_b32_e32 v30, v17
	v_mov_b32_e32 v29, v17
	v_mov_b32_e32 v28, v17
	v_mov_b32_e32 v27, v17
	v_mov_b32_e32 v26, v17
	v_mov_b32_e32 v25, v17
	v_mov_b32_e32 v24, v17
	v_mov_b32_e32 v23, v17
	v_mov_b32_e32 v22, v17
	v_mov_b32_e32 v21, v17
	v_mov_b32_e32 v20, v17
	v_mov_b32_e32 v19, v17
	v_mov_b32_e32 v18, v17
	v_mov_b32_e32 v140, v17
	v_mov_b32_e32 v202, v17
	s_addk_i32 s2, 0x2000
	s_add_i32 s94, s94, 1
	s_cmp_eq_u32 s87, s2
	s_cbranch_scc1 .LBB0_2467

.LBB0_2429:
	s_cmp_gt_u32 s78, s92
	s_cselect_b64 s[78:79], -1, 0
	s_and_b64 s[78:79], s[78:79], exec
	s_cselect_b32 s79, s93, 0
	s_cselect_b32 s78, s96, 0xa00
	s_add_i32 s79, s79, s3
	s_lshl_b32 s79, s79, 6
	s_addk_i32 s79, 0xc0
	s_mul_hi_i32 s81, s79, 0x4e00
	s_mulk_i32 s79, 0x4e00
	s_add_u32 s79, s0, s79
	s_addc_u32 s81, s1, s81
	s_add_u32 s78, s79, s78
	s_addc_u32 s79, s81, 0
	v_lshl_add_u64 v[222:223], s[78:79], 0, v[130:131]
	s_add_i32 s78, s2, 0x6000
	s_and_b32 s78, s78, 0x6000
	s_add_i32 s78, s78, s75
	s_mov_b32 s79, m0
	s_mov_b32 m0, s78
	s_nop 0
	global_load_lds_dwordx4 v[222:223], off
	s_mov_b32 m0, s79
	s_andn2_b64 vcc, exec, s[72:73]
	s_cbranch_vccz .LBB0_2433
	s_branch .LBB0_2434

.LBB0_2433:
	s_mul_hi_u32 s72, s94, 0xaaaaaaab
	s_lshr_b32 s72, s72, 1
	s_mulk_i32 s72, 0x6000
	s_sub_i32 s78, s86, s72
	s_cmp_gt_u32 s80, s92
	s_cselect_b64 s[72:73], -1, 0
	s_and_b64 s[72:73], s[72:73], exec
	s_movk_i32 s72, 0x1c00
	s_cselect_b32 s73, s93, 0
	s_cselect_b32 s72, s72, 0x1a00
	s_add_i32 s73, s73, s3
	s_lshl_b32 s73, s73, 6
	s_addk_i32 s73, 0x80
	s_mul_hi_i32 s79, s73, 0x4e00
	s_mulk_i32 s73, 0x4e00
	s_add_u32 s73, s0, s73
	s_addc_u32 s79, s1, s79
	s_add_u32 s72, s73, s72
	s_addc_u32 s73, s79, 0
	v_lshl_add_u64 v[222:223], s[72:73], 0, v[138:139]
	s_add_i32 s72, s2, s78
	s_mov_b32 s73, m0
	s_mov_b32 m0, s72
	s_nop 0
	global_load_lds_dwordx4 v[222:223], off
	s_mov_b32 m0, s73
.LBB0_2434:
	s_cmp_gt_u32 s3, s92
	s_cselect_b64 s[72:73], -1, 0
	s_mov_b64 s[78:79], 0
	s_and_b64 vcc, exec, s[72:73]
	s_cbranch_vccnz .LBB0_2436
	ds_read_b32 v222, v183 offset:57856
	s_waitcnt lgkmcnt(0)
	v_not_b32_e32 v222, v222
	v_lshrrev_b32_e32 v222, s3, v222
	v_and_b32_e32 v222, 1, v222
	v_cmp_eq_u32_e32 vcc, 1, v222
	s_and_b64 s[78:79], vcc, exec
.LBB0_2436:
	v_cndmask_b32_e64 v222, 0, 1, s[78:79]
	v_cmp_ne_u32_e32 vcc, 0, v222
	s_cmp_lg_u64 vcc, 0
	s_cselect_b64 s[80:81], -1, 0
	s_and_b32 s82, s2, 0x6000
	v_add_u32_e32 v224, s82, v182
	ds_read_b128 v[228:231], v224 offset:512
	ds_read_b128 v[232:235], v224 offset:2560
	ds_read_b128 v[236:239], v224 offset:4608
	ds_read_b128 v[240:243], v224 offset:6656
	s_waitcnt lgkmcnt(3)
	v_mfma_f32_32x32x16_bf16 v[82:97], v[228:231], v[114:117], v[34:49]
	s_waitcnt lgkmcnt(2)
	v_mfma_f32_32x32x16_bf16 v[82:97], v[232:235], v[118:121], v[82:97]
	s_waitcnt lgkmcnt(1)
	v_mfma_f32_32x32x16_bf16 v[82:97], v[236:239], v[122:125], v[82:97]
	s_waitcnt lgkmcnt(0)
	v_mfma_f32_32x32x16_bf16 v[82:97], v[240:243], v[126:129], v[82:97]
	ds_read_b64_tr_b16 v[228:229], v225
	ds_read_b64_tr_b16 v[230:231], v225 offset:512
	ds_read_b64_tr_b16 v[232:233], v225 offset:1024
	ds_read_b64_tr_b16 v[234:235], v225 offset:1536
	ds_read_b64_tr_b16 v[236:237], v225 offset:4096
	ds_read_b64_tr_b16 v[238:239], v225 offset:4608
	ds_read_b64_tr_b16 v[240:241], v225 offset:5120
	ds_read_b64_tr_b16 v[242:243], v225 offset:5632
	s_cbranch_vccz .LBB0_2438
	v_cndmask_b32_e64 v50, v50, v1, s[78:79]
	v_cndmask_b32_e64 v51, v51, v1, s[78:79]
	v_cndmask_b32_e64 v52, v52, v1, s[78:79]
	v_cndmask_b32_e64 v53, v53, v1, s[78:79]
	v_cndmask_b32_e64 v54, v54, v1, s[78:79]
	v_cndmask_b32_e64 v55, v55, v1, s[78:79]
	v_cndmask_b32_e64 v56, v56, v1, s[78:79]
	v_cndmask_b32_e64 v57, v57, v1, s[78:79]
	v_cndmask_b32_e64 v58, v58, v1, s[78:79]
	v_cndmask_b32_e64 v59, v59, v1, s[78:79]
	v_cndmask_b32_e64 v60, v60, v1, s[78:79]
	v_cndmask_b32_e64 v61, v61, v1, s[78:79]
	v_cndmask_b32_e64 v62, v62, v1, s[78:79]
	v_cndmask_b32_e64 v63, v63, v1, s[78:79]
	v_cndmask_b32_e64 v64, v64, v1, s[78:79]
	v_cndmask_b32_e64 v65, v65, v1, s[78:79]
.LBB0_2438:
	s_and_b64 s[82:83], exec, s[72:73]
	s_cselect_b32 s82, s93, 0
	s_sub_i32 s82, s92, s82
	s_add_i32 s84, s82, -8
	s_cmp_lg_u32 s82, s3
	s_cselect_b64 s[82:83], -1, 0
	s_cmp_eq_u32 s84, s3
	s_cselect_b64 s[84:85], -1, 0
	s_and_b64 s[72:73], s[72:73], s[84:85]
	v_cndmask_b32_e64 v222, 0, 1, s[72:73]
	s_mov_b64 s[84:85], -1
	s_and_b64 vcc, exec, s[82:83]
	v_cmp_ne_u32_e64 s[72:73], 1, v222
	s_cbranch_vccz .LBB0_2442
	s_and_b64 vcc, exec, s[72:73]
	s_cbranch_vccnz .LBB0_2441
	v_cndmask_b32_e64 v50, v1, v50, s[6:7]
	v_cndmask_b32_e64 v51, v51, v1, s[8:9]
	v_cndmask_b32_e64 v52, v1, v52, s[10:11]
	v_cndmask_b32_e64 v53, v1, v53, s[12:13]
	v_cndmask_b32_e64 v54, v1, v54, s[14:15]
	v_cndmask_b32_e64 v55, v1, v55, s[16:17]
	v_cndmask_b32_e64 v56, v1, v56, s[18:19]
	v_cndmask_b32_e64 v57, v1, v57, s[20:21]
	v_cndmask_b32_e64 v58, v1, v58, s[22:23]
	v_cndmask_b32_e64 v59, v1, v59, s[24:25]
	v_cndmask_b32_e64 v60, v1, v60, s[26:27]
	v_cndmask_b32_e64 v61, v1, v61, s[28:29]
	v_cndmask_b32_e64 v62, v1, v62, s[30:31]
	v_cndmask_b32_e64 v63, v1, v63, s[34:35]
	v_cndmask_b32_e64 v64, v1, v64, s[36:37]
	v_cndmask_b32_e64 v65, v1, v65, s[38:39]

.LBB0_2442:
	s_andn2_b64 vcc, exec, s[84:85]
	s_cbranch_vccnz .LBB0_2444
	v_mov_b32_e32 v210, v50
	v_cndmask_b32_e64 v50, v50, v1, s[6:7]
	v_cndmask_b32_e64 v51, v1, v51, s[8:9]
	v_cndmask_b32_e64 v50, v50, v210, s[8:9]
	v_cndmask_b32_e64 v52, v52, v1, s[10:11]
	v_cndmask_b32_e64 v53, v53, v1, s[12:13]
	v_cndmask_b32_e64 v54, v54, v1, s[14:15]
	v_cndmask_b32_e64 v55, v55, v1, s[16:17]
	v_cndmask_b32_e64 v56, v56, v1, s[18:19]
	v_cndmask_b32_e64 v57, v57, v1, s[20:21]
	v_cndmask_b32_e64 v58, v58, v1, s[22:23]
	v_cndmask_b32_e64 v59, v59, v1, s[24:25]
	v_cndmask_b32_e64 v60, v60, v1, s[26:27]
	v_cndmask_b32_e64 v61, v61, v1, s[28:29]
	v_cndmask_b32_e64 v62, v62, v1, s[30:31]
	v_cndmask_b32_e64 v63, v63, v1, s[34:35]
	v_cndmask_b32_e64 v64, v64, v1, s[36:37]
	v_cndmask_b32_e64 v65, v65, v1, s[38:39]

.LBB0_2448:
	v_exp_f32_e32 v142, v50
	v_exp_f32_e32 v143, v51
	v_exp_f32_e32 v144, v52
	v_exp_f32_e32 v145, v53
	v_exp_f32_e32 v146, v54
	v_exp_f32_e32 v147, v55
	v_exp_f32_e32 v148, v56
	v_exp_f32_e32 v149, v57
	v_exp_f32_e32 v150, v58
	v_exp_f32_e32 v151, v59
	v_exp_f32_e32 v152, v60
	v_exp_f32_e32 v153, v61
	v_exp_f32_e32 v154, v62
	v_exp_f32_e32 v155, v63
	v_exp_f32_e32 v156, v64
	v_exp_f32_e32 v157, v65
	s_branch .Lnsa_pv0_cvt

.Lnsa_pv0_cvt:
	v_cvt_pk_bf16_f32 v98, v142, v143
	v_cvt_pk_bf16_f32 v99, v144, v145
	v_cvt_pk_bf16_f32 v100, v146, v147
	v_cvt_pk_bf16_f32 v101, v148, v149
	v_cvt_pk_bf16_f32 v102, v150, v151
	v_cvt_pk_bf16_f32 v103, v152, v153
	v_cvt_pk_bf16_f32 v104, v154, v155
	v_cvt_pk_bf16_f32 v105, v156, v157
	s_add_i32 s3, s3, 1
	s_waitcnt lgkmcnt(0)
	v_mfma_f32_32x32x16_bf16 v[2:17], v[98:101], v[228:231], v[2:17]
	v_mfma_f32_32x32x16_bf16 v[2:17], v[102:105], v[232:235], v[2:17]
	v_mfma_f32_32x32x16_bf16 v[18:33], v[98:101], v[236:239], v[18:33]
	v_mfma_f32_32x32x16_bf16 v[18:33], v[102:105], v[240:243], v[18:33]
	s_cmp_ge_u32 s3, s90
	s_cbranch_scc1 .LBB0_2451
	s_add_i32 s85, s2, 0x2000
	s_and_b32 s85, s85, 0x6000
	v_add_u32_e32 v102, s85, v182
	ds_read_b128 v[228:231], v102
	ds_read_b128 v[232:235], v102 offset:2048
	ds_read_b128 v[236:239], v102 offset:4096
	ds_read_b128 v[240:243], v102 offset:6144
	s_waitcnt lgkmcnt(3)
	v_mfma_f32_32x32x16_bf16 v[50:65], v[228:231], v[114:117], v[34:49]
	s_waitcnt lgkmcnt(2)
	v_mfma_f32_32x32x16_bf16 v[50:65], v[232:235], v[118:121], v[50:65]
	s_waitcnt lgkmcnt(1)
	v_mfma_f32_32x32x16_bf16 v[50:65], v[236:239], v[122:125], v[50:65]
	s_waitcnt lgkmcnt(0)
	v_mfma_f32_32x32x16_bf16 v[50:65], v[240:243], v[126:129], v[50:65]

.LBB0_2466:
	s_addk_i32 s2, 0x2000
	s_add_i32 s94, s94, 1
	s_cmp_eq_u32 s87, s2
	s_cbranch_scc0 .LBB0_2422
